# attn: key-tile rotation (2qb+15head)&31
# speedup vs baseline: 1.0333x; 1.0333x over previous
.Lp_top:
	s_lshl_b32 s6, s21, 20
	s_add_u32 s4, s4, s6
	s_addc_u32 s5, s5, 0
	v_lshlrev_b32_e32 v54, 4, v0
	v_mov_b32_e32 v55, v63
	s_lshl_b32 s3, s3, 1
	s_mul_i32 s20, s21, 15
	v_lshl_add_u64 v[4:5], s[4:5], 0, v[54:55]
	s_mov_b64 s[4:5], 0x1000000
	s_add_i32 s20, s20, s3
	v_lshl_add_u64 v[170:171], v[4:5], 0, s[4:5]
	s_and_b32 s22, s20, 31
	s_lshl_b32 s4, s20, 12
	s_lshl_b32 s12, s22, 13
	s_add_i32 s5, s4, 0x1000
	v_lshl_add_u64 v[58:59], v[170:171], 0, s[12:13]
	s_mov_b32 s3, 0x80000
	s_and_b32 s5, s5, 0x1f000
	v_add_co_u32_e32 v16, vcc, s3, v58
	s_lshl_b32 s12, s5, 1
	s_nop 0
	v_addc_co_u32_e32 v17, vcc, 0, v59, vcc
	v_lshl_add_u64 v[56:57], v[170:171], 0, s[12:13]
	global_load_dwordx4 v[4:7], v[58:59], off
	global_load_dwordx4 v[8:11], v[56:57], off
	global_load_dwordx4 v[12:15], v[16:17], off
	v_add_co_u32_e32 v16, vcc, s3, v56
	v_lshrrev_b32_e32 v184, 8, v0
	s_nop 0
	v_addc_co_u32_e32 v17, vcc, 0, v57, vcc
	global_load_dwordx4 v[16:19], v[16:17], off
	v_and_b32_e32 v20, 19, v0
	v_lshlrev_b32_e32 v21, 1, v0
	v_and_b32_e32 v2, 4, v2
	v_and_or_b32 v20, v21, 8, v20
	v_lshlrev_b32_e32 v101, 5, v184
	s_addk_i32 s4, 0x2000
	v_or3_b32 v2, v20, v2, v101
	s_and_b32 s4, s4, 0x1f000
	v_mul_u32_u24_e32 v2, 0x48, v2
	s_lshl_b32 s12, s4, 1
	v_lshlrev_b32_e32 v3, 3, v0
	v_lshlrev_b32_e32 v100, 1, v99
	v_lshlrev_b32_e32 v2, 1, v2
	v_lshl_add_u64 v[60:61], v[170:171], 0, s[12:13]
	v_and_b32_e32 v3, 56, v3
	v_add3_u32 v186, 0, v2, v100
	v_add_co_u32_e32 v2, vcc, s3, v60
	v_lshlrev_b32_e32 v68, 1, v3
	s_nop 0
	v_addc_co_u32_e32 v3, vcc, 0, v61, vcc
	global_load_dwordx4 v[162:165], v[60:61], off
	global_load_dwordx4 v[166:169], v[2:3], off
	v_lshrrev_b32_e32 v82, 3, v0
	v_mul_u32_u24_e32 v22, 0x48, v82
	v_lshlrev_b32_e32 v21, 1, v22
	v_add3_u32 v185, 0, v21, v68
	s_mov_b64 s[24:25], 0x80000
	s_add_i32 s17, s20, 3
	s_add_i32 s18, s20, 4
	v_mov_b32_e32 v62, v63
	v_lshrrev_b32_e32 v55, 6, v0
	v_mov_b32_e32 v83, 0
	v_mov_b32_e32 v84, 0
	v_lshl_add_u64 v[70:71], v[58:59], 0, s[24:25]
	v_lshl_add_u64 v[66:67], v[56:57], 0, s[24:25]
	v_lshl_add_u64 v[64:65], v[60:61], 0, s[24:25]
	s_waitcnt vmcnt(5)
	ds_write_b128 v185, v[4:7]
	s_waitcnt vmcnt(3)
	ds_write_b128 v185, v[12:15] offset:9216
	ds_write_b128 v185, v[8:11] offset:18432
	s_waitcnt vmcnt(2)
	ds_write_b128 v185, v[16:19] offset:27648
	s_waitcnt lgkmcnt(0)
	s_barrier
	ds_read_b128 v[2:5], v186
	ds_read_b128 v[38:41], v186 offset:32
	s_waitcnt lgkmcnt(1)
	v_mfma_f32_32x32x16_f16 v[2:17], v[2:5], v[114:117], 0
	ds_read_b128 v[18:21], v186 offset:9216
	ds_read_b128 v[46:49], v186 offset:9248
	s_waitcnt lgkmcnt(1)
	v_mfma_f32_32x32x16_f16 v[18:33], v[18:21], v[130:133], 0
	v_mfma_f32_32x32x16_f16 v[2:17], v[38:41], v[118:121], v[2:17]
	s_waitcnt lgkmcnt(0)
	v_mfma_f32_32x32x16_f16 v[18:33], v[46:49], v[134:137], v[18:33]
	ds_read_b128 v[38:41], v186 offset:64
	ds_read_b128 v[46:49], v186 offset:96
	s_waitcnt lgkmcnt(1)
	v_mfma_f32_32x32x16_f16 v[2:17], v[38:41], v[122:125], v[2:17]
	ds_read_b128 v[38:41], v186 offset:9280
	ds_read_b128 v[50:53], v186 offset:9312
	s_load_dwordx4 s[4:7], s[0:1], 0x38
	s_load_dwordx2 s[14:15], s[0:1], 0x8
	s_mov_b32 s0, -2
	s_mov_b32 s1, 0x3f800000
	s_waitcnt lgkmcnt(0)
	s_barrier
	v_mfma_f32_32x32x16_f16 v[18:33], v[38:41], v[138:141], v[18:33]
	v_mfma_f32_32x32x16_f16 v[2:17], v[46:49], v[126:129], v[2:17]
	v_mfma_f32_32x32x16_f16 v[18:33], v[50:53], v[142:145], v[18:33]
	s_lshl_b32 s12, s17, 13
	s_and_b32 s12, s12, 0x3e000
	s_add_u32 s28, s12, s3
	s_mov_b32 s29, 0
	v_lshl_add_u64 v[176:177], v[170:171], 0, s[12:13]
	global_load_dwordx4 v[50:53], v[176:177], off
	v_lshl_add_u64 v[176:177], v[170:171], 0, s[28:29]
	global_load_dwordx4 v[94:97], v[176:177], off
	s_nop 7
	s_cmp_eq_u32 s37, 1
	s_cbranch_scc0 .Lf_A
	v_mov_b32_e32 v83, 0xf149f2ca
	v_mov_b32_e32 v84, 0xf149f2ca
	s_branch .Ls_A

.Ll1_cont:
	ds_bpermute_b32 v2, v69, v84
	ds_bpermute_b32 v5, v69, v83
	v_max_f32_e32 v4, v84, v84
	v_max_f32_e32 v7, v83, v83
	ds_bpermute_b32 v3, v69, v63
	s_waitcnt lgkmcnt(2)
	v_max_f32_e32 v6, v2, v2
	v_max_f32_e32 v4, v4, v6
	v_sub_f32_e32 v6, v84, v4
	v_exp_f32_e32 v9, v6
	s_waitcnt lgkmcnt(1)
	v_max_f32_e32 v6, v5, v5
	v_sub_f32_e32 v2, v2, v4
	v_max_f32_e32 v6, v7, v6
	v_exp_f32_e32 v11, v2
	ds_bpermute_b32 v2, v69, v62
	v_sub_f32_e32 v5, v5, v6
	v_sub_f32_e32 v7, v83, v6
	v_exp_f32_e32 v10, v5
	v_exp_f32_e32 v8, v7
	v_cmp_gt_u32_e32 vcc, 32, v98
	s_waitcnt lgkmcnt(0)
	v_pk_mul_f32 v[2:3], v[10:11], v[2:3]
	s_nop 0
	v_pk_fma_f32 v[8:9], v[62:63], v[8:9], v[2:3]
	v_lshlrev_b32_e32 v2, 7, v184
	v_or3_b32 v10, v183, v2, v1
	s_and_saveexec_b64 s[0:1], vcc
	v_lshl_add_u32 v2, v10, 4, 0
	v_add_u32_e32 v2, 0x21000, v2
	v_mov_b32_e32 v5, v9
	v_mov_b32_e32 v7, v8
	ds_write_b128 v2, v[4:7]
	s_or_b64 exec, exec, s[0:1]
	s_lshl_b32 s12, s21, 7
	s_mov_b32 s3, 0
	v_or_b32_e32 v2, s12, v82
	s_lshl_b32 s13, s21, 11
	s_add_i32 s23, 0, 0x12000
	v_lshlrev_b32_e32 v2, 12, v2
	v_mov_b32_e32 v3, 0
	s_add_i32 s13, s13, s16
	s_lshl_b64 s[0:1], s[2:3], 13
	v_lshl_add_u64 v[12:13], s[14:15], 0, v[2:3]
	v_mov_b32_e32 v69, v3
	s_add_u32 s0, s10, s0
	v_lshl_add_u64 v[172:173], v[12:13], 0, v[68:69]
	s_addc_u32 s1, s11, s1
	s_lshl_b32 s10, s22, 7
	s_mov_b32 s11, s3
	s_waitcnt vmcnt(1)
	v_lshl_add_u64 v[36:37], v[172:173], 0, s[10:11]
	s_mov_b32 s10, 0x40000
	v_add_co_u32_e32 v38, vcc, s10, v36
	s_waitcnt lgkmcnt(0)
	s_barrier
	global_load_dwordx4 v[12:15], v[58:59], off
	global_load_dwordx4 v[16:19], v[70:71], off
	v_addc_co_u32_e32 v39, vcc, 0, v37, vcc
	global_load_dwordx4 v[20:23], v[56:57], off
	global_load_dwordx4 v[24:27], v[66:67], off
	global_load_dwordx4 v[28:31], v[36:37], off
	global_load_dwordx4 v[32:35], v[38:39], off
	v_add_f32_e32 v2, v78, v80
	s_movk_i32 s11, 0x1200
	v_add_f32_e32 v5, v79, v81
	s_mov_b32 s14, 0x3fb8aa3b
	v_lshlrev_b32_e32 v10, 4, v10
	v_mov_b32_e32 v36, s23
	v_mul_f32_e32 v37, 0x3fb8aa3b, v2
	v_mul_f32_e32 v38, 0x3fb8aa3b, v5
	v_xor_b32_e32 v10, 0x800, v10
	v_mad_u32_u24 v40, v55, s11, v36
	v_fma_f32 v36, v2, s14, -v37
	v_rndne_f32_e32 v39, v37
	v_fma_f32 v41, v5, s14, -v38
	s_waitcnt vmcnt(6)
	v_rndne_f32_e32 v42, v38
	v_add_u32_e32 v10, 0, v10
	v_fmac_f32_e32 v36, 0x32a5705f, v2
	v_sub_f32_e32 v37, v37, v39
	v_fmac_f32_e32 v41, 0x32a5705f, v5
	v_sub_f32_e32 v38, v38, v42
	v_add_u32_e32 v10, 0x21000, v10
	v_add_f32_e32 v44, v37, v36
	global_load_dwordx4 v[146:149], v[60:61], off
	global_load_dwordx4 v[150:153], v[64:65], off
	v_cvt_i32_f32_e32 v43, v39
	v_add_f32_e32 v41, v38, v41
	ds_read_b128 v[36:39], v10
	v_exp_f32_e32 v10, v44
	v_cvt_i32_f32_e32 v42, v42
	v_exp_f32_e32 v41, v41
	s_mov_b32 s21, 0xc2ce8ed0
	s_lshl_b32 s11, s20, 6
	s_add_i32 s14, s11, 64
	v_ldexp_f32 v10, v10, v43
	v_cmp_ngt_f32_e32 vcc, s21, v2
	s_mov_b32 s22, 0x42b17218
	s_and_b32 s14, s14, 0x7c0
	v_ldexp_f32 v41, v41, v42
	v_cndmask_b32_e32 v10, 0, v10, vcc
	v_cmp_ngt_f32_e32 vcc, s21, v5
	v_mov_b32_e32 v7, 0x7f800000
	v_max_f32_e32 v11, v4, v4
	s_mov_b32 s15, s3
	s_lshl_b32 s14, s14, 1
	s_waitcnt lgkmcnt(0)
	v_max_f32_e32 v42, v36, v36
	v_cndmask_b32_e32 v41, 0, v41, vcc
	v_cmp_nlt_f32_e32 vcc, s22, v2
	v_max_f32_e32 v187, v11, v42
	v_mov_b32_e32 v55, v3
	v_cndmask_b32_e32 v2, v7, v10, vcc
	v_cmp_nlt_f32_e32 vcc, s22, v5
	v_lshl_add_u64 v[10:11], v[172:173], 0, s[14:15]
	v_lshl_add_u64 v[178:179], s[0:1], 0, v[54:55]
	v_cndmask_b32_e32 v5, v7, v41, vcc
	v_sub_f32_e32 v2, v2, v5
	v_add_f32_e32 v41, 0x3e4ccccd, v2
	v_sub_f32_e32 v2, v4, v187
	v_max_f32_e32 v4, v6, v6
	s_and_b32 s1, s2, 7
	s_mulk_i32 s1, 0x780
	s_mulk_i32 s19, 0x3c0
	s_add_i32 s0, s20, 2
	s_waitcnt vmcnt(7)
	ds_write_b128 v185, v[12:15]
	s_waitcnt vmcnt(6)
	ds_write_b128 v185, v[16:19] offset:9216
	s_waitcnt vmcnt(5)
	ds_write_b128 v185, v[20:23] offset:18432
	s_waitcnt vmcnt(4)
	ds_write_b128 v185, v[24:27] offset:27648
	s_waitcnt vmcnt(3)
	ds_write_b128 v185, v[28:31] offset:36864
	s_waitcnt vmcnt(2)
	ds_write_b128 v185, v[32:35] offset:46080
	v_add_co_u32_e32 v12, vcc, s10, v10
	v_exp_f32_e32 v23, v2
	s_nop 0
	v_addc_co_u32_e32 v13, vcc, 0, v11, vcc
	global_load_dwordx4 v[154:157], v[10:11], off
	global_load_dwordx4 v[158:161], v[12:13], off
	s_waitcnt lgkmcnt(0)
	s_barrier
	ds_read_b128 v[10:13], v186
	v_sub_f32_e32 v2, v36, v187
	v_exp_f32_e32 v25, v2
	v_max_f32_e32 v2, v38, v38
	v_max_f32_e32 v188, v4, v2
	v_sub_f32_e32 v2, v6, v188
	v_exp_f32_e32 v22, v2
	v_sub_f32_e32 v2, v38, v188
	v_exp_f32_e32 v24, v2
	ds_read_b128 v[14:17], v186 offset:9216
	ds_read_b128 v[18:21], v186 offset:32
	s_waitcnt lgkmcnt(2)
	v_mfma_f32_32x32x16_f16 v[66:81], v[10:13], v[114:117], 0
	v_mov_b32_e32 v36, v39
	v_mul_f32_e64 v10, v36, v24
	v_mul_f32_e64 v11, v37, v25
	ds_read_b128 v[4:7], v186 offset:9248
	s_add_i32 s1, s1, s19
	s_mov_b32 s14, 0x30000
	s_mov_b32 s15, 0x80000
	s_mov_b32 s19, 0
	s_waitcnt lgkmcnt(2)
	v_mfma_f32_32x32x16_f16 v[82:97], v[14:17], v[130:133], 0
	v_fma_f32 v16, v8, v22, v10
	v_fma_f32 v17, v9, v23, v11
	v_log_f32_e32 v238, v17
	s_nop 0
	v_add_f32_e32 v187, v187, v238
	v_sub_f32_e32 v240, 0, v187
	v_sub_f32_e32 v241, 0, v187
	v_sub_f32_e32 v242, 0, v187
	v_sub_f32_e32 v243, 0, v187
	v_sub_f32_e32 v244, 0, v187
	v_sub_f32_e32 v245, 0, v187
	v_sub_f32_e32 v246, 0, v187
	v_sub_f32_e32 v247, 0, v187
	v_sub_f32_e32 v248, 0, v187
	v_sub_f32_e32 v249, 0, v187
	v_sub_f32_e32 v250, 0, v187
	v_sub_f32_e32 v251, 0, v187
	v_sub_f32_e32 v252, 0, v187
	v_sub_f32_e32 v253, 0, v187
	v_sub_f32_e32 v254, 0, v187
	v_sub_f32_e32 v255, 0, v187
	v_lshrrev_b32_e32 v22, 3, v98
	v_or3_b32 v2, s13, v183, v22
	v_lshlrev_b64 v[8:9], 13, v[2:3]
	v_lshl_add_u64 v[8:9], s[4:5], 0, v[8:9]
	v_lshlrev_b32_e32 v2, 2, v101
	v_lshl_add_u64 v[8:9], v[8:9], 0, v[2:3]
	v_and_b32_e32 v2, 0x70, v54
	v_lshl_add_u64 v[174:175], v[8:9], 0, v[2:3]
	ds_read_b128 v[8:11], v186 offset:64
	s_waitcnt lgkmcnt(2)
	v_mfma_f32_32x32x16_f16 v[66:81], v[18:21], v[118:121], v[66:81]
	v_div_scale_f32 v18, s[4:5], v16, v16, -v41
	v_rcp_f32_e32 v19, v18
	v_div_scale_f32 v20, vcc, -v41, v16, -v41
	s_mov_b32 s13, 0x20000
	v_mov_b32_e32 v24, v3
	s_waitcnt lgkmcnt(1)
	v_mfma_f32_32x32x16_f16 v[82:97], v[4:7], v[134:137], v[82:97]
	v_fma_f32 v4, -v18, v19, 1.0
	v_fmac_f32_e32 v19, v4, v19
	v_mul_f32_e32 v21, v20, v19
	ds_read_b128 v[4:7], v186 offset:9280
	ds_read_b128 v[12:15], v186 offset:96
	v_mov_b32_e32 v25, v3
	v_mov_b32_e32 v26, v3
	v_mov_b32_e32 v27, v3
	s_waitcnt lgkmcnt(2)
	v_mfma_f32_32x32x16_f16 v[66:81], v[8:11], v[122:125], v[66:81]
	v_fma_f32 v8, -v18, v21, v20
	v_fmac_f32_e32 v21, v8, v19
	v_fma_f32 v18, -v18, v21, v20
	v_div_scale_f32 v20, s[4:5], v17, v17, 1.0
	v_rcp_f32_e32 v23, v20
	ds_read_b128 v[8:11], v186 offset:9312
	s_waitcnt lgkmcnt(2)
	v_mfma_f32_32x32x16_f16 v[82:97], v[4:7], v[138:141], v[82:97]
	v_div_fmas_f32 v4, v18, v19, v21
	v_div_fixup_f32 v176, v4, v16, -v41
	v_fma_f32 v4, -v20, v23, 1.0
	v_fmac_f32_e32 v23, v4, v23
	v_div_scale_f32 v4, vcc, 1.0, v17, 1.0
	v_mul_f32_e32 v5, v4, v23
	v_fma_f32 v6, -v20, v5, v4
	v_fmac_f32_e32 v5, v6, v23
	s_waitcnt lgkmcnt(1)
	v_mfma_f32_32x32x16_f16 v[66:81], v[12:15], v[126:129], v[66:81]
	v_fma_f32 v4, -v20, v5, v4
	v_div_fmas_f32 v4, v4, v23, v5
	v_div_fixup_f32 v177, v4, v17, 1.0
	v_mul_u32_u24_e32 v4, 0x90, v22
	v_add3_u32 v189, v40, v4, v2
	v_mul_u32_u24_e32 v2, 0x90, v1
	v_lshlrev_b32_e32 v4, 2, v99
	s_waitcnt lgkmcnt(0)
	v_mfma_f32_32x32x16_f16 v[82:97], v[8:11], v[142:145], v[82:97]
	v_add3_u32 v190, v40, v2, v4
	v_mul_u32_u24_e32 v2, 0x48, v1
	v_lshl_add_u32 v2, v2, 1, 0
	v_lshlrev_b32_e32 v4, 1, v101
	v_add3_u32 v191, v2, v4, v100
	s_mov_b32 s4, 0x3f800000
	s_mov_b32 s5, 0x10000
	v_mov_b32_e32 v2, v3
	v_mov_b32_e32 v4, v3
	v_mov_b32_e32 v5, v3
	v_mov_b32_e32 v6, v3
	v_mov_b32_e32 v7, v3
	v_mov_b32_e32 v8, v3
	v_mov_b32_e32 v9, v3
	v_mov_b32_e32 v10, v3
	v_mov_b32_e32 v11, v3
	v_mov_b32_e32 v12, v3
	v_mov_b32_e32 v13, v3
	v_mov_b32_e32 v14, v3
	v_mov_b32_e32 v15, v3
	v_mov_b32_e32 v16, v3
	v_mov_b32_e32 v17, v3
	v_mov_b32_e32 v18, v3
	v_mov_b32_e32 v19, v3
	v_mov_b32_e32 v20, v3
	v_mov_b32_e32 v21, v3
	v_mov_b32_e32 v22, v3
	v_mov_b32_e32 v23, v3
	v_mov_b32_e32 v28, v3
	v_mov_b32_e32 v29, v3
	v_mov_b32_e32 v30, v3
	v_mov_b32_e32 v31, v3
	v_mov_b32_e32 v32, v3
	v_mov_b32_e32 v33, v3
	v_mov_b32_e32 v34, v3
	v_mov_b32_e32 v35, v3
	v_mov_b32_e32 v36, v3
	v_mov_b32_e32 v37, v3
	v_mov_b32_e32 v38, v3
	v_mov_b32_e32 v39, v3
	v_mov_b32_e32 v40, v3
	v_mov_b32_e32 v41, v3
	v_mov_b32_e32 v42, v3
	v_mov_b32_e32 v43, v3
	v_mov_b32_e32 v44, v3
	v_mov_b32_e32 v45, v3
	v_mov_b32_e32 v46, v3
	v_mov_b32_e32 v47, v3
	v_mov_b32_e32 v48, v3
	v_mov_b32_e32 v49, v3
	v_mov_b32_e32 v50, v3
	v_mov_b32_e32 v51, v3
	v_mov_b32_e32 v52, v3
	v_mov_b32_e32 v53, v3
	v_mov_b32_e32 v54, v3
	v_mov_b32_e32 v56, v3
	v_mov_b32_e32 v57, v3
	v_mov_b32_e32 v58, v3
	v_mov_b32_e32 v59, v3
	v_mov_b32_e32 v60, v3
	v_mov_b32_e32 v61, v3
	v_mov_b32_e32 v62, v3
	v_mov_b32_e32 v63, v3
	v_mov_b32_e32 v64, v3
	v_mov_b32_e32 v65, v3
	v_add_u32_e32 v192, 0xd800, v191
	v_sub_f32_e32 v66, v66, v187
	v_sub_f32_e32 v67, v67, v187
	v_sub_f32_e32 v68, v68, v187
	v_sub_f32_e32 v69, v69, v187
	v_sub_f32_e32 v70, v70, v187
	v_sub_f32_e32 v71, v71, v187
	v_sub_f32_e32 v72, v72, v187
	v_sub_f32_e32 v73, v73, v187
	v_sub_f32_e32 v74, v74, v187
	v_sub_f32_e32 v75, v75, v187
	v_sub_f32_e32 v76, v76, v187
	v_sub_f32_e32 v77, v77, v187
	v_sub_f32_e32 v78, v78, v187
	v_sub_f32_e32 v79, v79, v187
	v_sub_f32_e32 v80, v80, v187
	v_sub_f32_e32 v81, v81, v187
	s_mov_b32 s27, 0x42c80000
	v_cmp_gt_f32_e64 vcc, |v188|, s27
	s_cbranch_vccnz .Ll2_gen
	v_sub_f32_e32 v238, 0, v188
	v_exp_f32_e32 v238, v238
	s_nop 0
	v_mul_f32_e32 v176, v176, v238
	s_barrier
	s_branch .Ll2f_top
